# v42 + MoE pre-phase block-order ranking loop: v_readlane broadcast instead of a ds_bpermute round trip per iteration (DPP/lane ops instead of LDS round trips)
# speedup vs baseline: 1.0044x; 1.0044x over previous
; __global__ void __launch_bounds__(NWAVES * 64, 2) mega_fwd(KArgs args) {
;     ...
;                 const int NF = __shfl(inc, 31, 32), fpos = inc - F; int rank = 0;
; #pragma unroll 1
;                 for (int k = 0; k < 32; ++k) { const int rk = __shfl(rem, k, 32); rank += (rk > rem || (rk == rem && rk > 0 && k < e)) ? 1 : 0; }
;                 if (lane < 32) { for (int j = 0; j < F; ++j) ordL[fpos + j] = (unsigned short)(pb + j); if (rem) ordL[NF + rank] = (unsigned short)(pb + F); }
.LBB0_1894:
	v_readlane_b32 s7, v37, s4
	v_mov_b32_e32 v5, 1
	s_nop 1
	v_mov_b32_e32 v6, s7
	v_cmp_le_i32_e64 s[22:23], v6, v37
	s_and_saveexec_b64 s[12:13], s[22:23]
	s_cbranch_execz .LBB0_1893
	v_cmp_eq_u32_e64 s[22:23], v6, v37
	v_cmp_lt_i32_e64 s[24:25], 0, v6
	s_and_b64 s[6:7], s[22:23], s[24:25]
	v_cmp_lt_u32_e64 s[22:23], s4, v4
	s_and_b64 s[6:7], s[6:7], s[22:23]
	v_cndmask_b32_e64 v5, 0, 1, s[6:7]
	s_branch .LBB0_1893
